# strategy 1 (wait/first-consumer placement): chain deferred Y store and its guard moved behind the first MFMA of the step; plus v_mov_b64 accumulator zeroing in the dense GEMM units
# baseline (speedup 1.0000x reference)
; #define LAS __attribute__((address_space(3)))
; DI unsigned cvt2(float lo, float hi) { return __builtin_bit_cast(unsigned, __builtin_convertvector((f32x2){lo, hi}, bfv2)); }
; DI void phase_chain(const Frame& F) {
;     ...
;             for (int jj = 0; jj < NSUB; ++jj) {
;                 __builtin_amdgcn_s_barrier(); asm volatile("" ::: "memory");
;                 const LAS unsigned char* st = ring + cur * CH_STB;
;                 bf16x8 sb[4]; sb[0] = pack8(S0, 0); sb[1] = pack8(S0, 1); sb[2] = pack8(S1, 0); sb[3] = pack8(S1, 1);
;                 const bf16x8 vt = *(const LAS bf16x8*)(st + 12800 + r * 32 + h * 16), wh = *(const LAS bf16x8*)(st + 12288 + rs * 32 + h * 16);
;                 const bf16x8 kh0 = *(const LAS bf16x8*)(st + 8192 + r * 32 + h * 16), kh1 = *(const LAS bf16x8*)(st + 8192 + (32 + r) * 32 + h * 16);
;                 f32x16 Y, N0, N1;
; #pragma unroll
;                 for (int i = 0; i < 16; ++i) { Y[i] = 0.f; N0[i] = 0.f; N1[i] = 0.f; }
;                 Y = __builtin_amdgcn_mfma_f32_32x32x16_bf16(wh, vt, Y, 0, 0, 0);
;                 N0 = __builtin_amdgcn_mfma_f32_32x32x16_bf16(kh0, vt, N0, 0, 0, 0);
;                 N1 = __builtin_amdgcn_mfma_f32_32x32x16_bf16(kh1, vt, N1, 0, 0, 0);
; #pragma unroll
;                 for (int ks = 0; ks < 4; ++ks) { const int c0 = ((4 * ks + h) ^ rs) * 8, c1 = ((4 * ks + h + 2) ^ rs) * 8;
;                     Y = __builtin_amdgcn_mfma_f32_32x32x16_bf16(cat8(st + 10240 + rs * 128 + c0, st + 10240 + rs * 128 + c1), sb[ks], Y, 0, 0, 0);
;                     N0 = __builtin_amdgcn_mfma_f32_32x32x16_bf16(cat8(st + r * 128 + c0, st + r * 128 + c1), sb[ks], N0, 0, 0, 0);
;                     N1 = __builtin_amdgcn_mfma_f32_32x32x16_bf16(cat8(st + (32 + r) * 128 + c0, st + (32 + r) * 128 + c1), sb[ks], N1, 0, 0, 0); }
;                 S0 = N0; S1 = N1;
; #pragma unroll
;                 for (int q = 0; q < 8; q += 1) { const int t = (q & 3) + 8 * (q >> 2) + 4 * h; *(LAS bf16_t*)(ybuf + (t * 32 + r) * 2) = (bf16_t)(cvt2(Y[q], 0.f) & 0xffffu); }
;                 { const u32x4 w = *(const LAS u32x4*)(ybuf + F.lane * 16); const int t = F.lane >> 2, step = 16 * jj + t, tt = d ? (SEQ - 1 - step) : step;
;                   *(u32x4*)(YD + ((size_t)d * T + (size_t)b * SEQ + tt) * 512 + hd * 64 + 32 * rb + 8 * (F.lane & 3)) = w; }
.LBB0_756:
	s_barrier
	ds_read_b128 v[134:137], v126 offset:12288
	ds_read_b128 v[138:141], v127 offset:12800
	ds_read_b128 v[142:145], v127 offset:8192
	ds_read_b128 v[146:149], v128 offset:8192
	ds_read_b64 v[150:151], v132 offset:10240
	ds_read_b64 v[152:153], v212 offset:10240
	v_cvt_pk_bf16_f32 v102, v16, v17
	v_cvt_pk_bf16_f32 v103, v18, v19
	v_cvt_pk_bf16_f32 v104, v20, v21
	v_cvt_pk_bf16_f32 v105, v22, v23
	v_cvt_pk_bf16_f32 v106, v24, v25
	v_cvt_pk_bf16_f32 v107, v26, v27
	v_cvt_pk_bf16_f32 v108, v28, v29
	v_cvt_pk_bf16_f32 v109, v30, v31
	v_cvt_pk_bf16_f32 v52, v0, v1
	v_cvt_pk_bf16_f32 v53, v2, v3
	v_cvt_pk_bf16_f32 v54, v4, v5
	v_cvt_pk_bf16_f32 v55, v6, v7
	v_cvt_pk_bf16_f32 v48, v8, v9
	v_cvt_pk_bf16_f32 v49, v10, v11
	v_cvt_pk_bf16_f32 v50, v12, v13
	v_cvt_pk_bf16_f32 v51, v14, v15
	s_waitcnt lgkmcnt(4)
	v_mfma_f32_32x32x16_bf16 v[32:47], v[134:137], v[138:141], 0
	s_cmpk_eq_i32 s4, 0xfff
	s_cbranch_scc1 .Lchain_nostore
	global_store_dwordx4 v[210:211], v[206:209], off
.Lchain_nostore:
	ds_read_b64 v[154:155], v213
	ds_read_b64 v[156:157], v214
	v_add_u32_e32 v215, v131, v83
	v_add_u32_e32 v216, v131, v84
	ds_read_b64 v[158:159], v215
	ds_read_b64 v[160:161], v216
	v_add_u32_e32 v215, v129, v85
	v_add_u32_e32 v216, v129, v86
	ds_read_b64 v[162:163], v215 offset:10240
	ds_read_b64 v[164:165], v216 offset:10240
	s_waitcnt lgkmcnt(9)
	v_mfma_f32_32x32x16_bf16 v[16:31], v[142:145], v[138:141], 0
	v_add_u32_e32 v215, v130, v85
	v_add_u32_e32 v216, v130, v86
	ds_read_b64 v[166:167], v215
	ds_read_b64 v[168:169], v216
	s_waitcnt lgkmcnt(10)
	v_mfma_f32_32x32x16_bf16 v[0:15], v[146:149], v[138:141], 0
	v_add_u32_e32 v215, v131, v85
	v_add_u32_e32 v216, v131, v86
	ds_read_b64 v[170:171], v215
	ds_read_b64 v[172:173], v216
	s_waitcnt lgkmcnt(10)
	v_mfma_f32_32x32x16_bf16 v[32:47], v[150:153], v[102:105], v[32:47]
	v_add_u32_e32 v215, v129, v87
	v_add_u32_e32 v216, v129, v88
	ds_read_b64 v[174:175], v215 offset:10240
	ds_read_b64 v[176:177], v216 offset:10240
	s_waitcnt lgkmcnt(10)
	v_mfma_f32_32x32x16_bf16 v[16:31], v[154:157], v[102:105], v[16:31]
	v_add_u32_e32 v215, v130, v87
	v_add_u32_e32 v216, v130, v88
	ds_read_b64 v[178:179], v215
	ds_read_b64 v[180:181], v216
	s_waitcnt lgkmcnt(10)
	v_mfma_f32_32x32x16_bf16 v[0:15], v[158:161], v[102:105], v[0:15]
	v_add_u32_e32 v215, v131, v87
	v_add_u32_e32 v216, v131, v88
	ds_read_b64 v[182:183], v215
	ds_read_b64 v[184:185], v216
	s_waitcnt lgkmcnt(10)
	v_mfma_f32_32x32x16_bf16 v[32:47], v[162:165], v[106:109], v[32:47]
	v_add_u32_e32 v215, v129, v89
	v_add_u32_e32 v216, v129, v90
	ds_read_b64 v[194:195], v215 offset:10240
	ds_read_b64 v[196:197], v216 offset:10240
	s_waitcnt lgkmcnt(10)
	v_mfma_f32_32x32x16_bf16 v[16:31], v[166:169], v[106:109], v[16:31]
	v_add_u32_e32 v215, v130, v89
	v_add_u32_e32 v216, v130, v90
	ds_read_b64 v[198:199], v215
	ds_read_b64 v[200:201], v216
	s_waitcnt lgkmcnt(10)
	v_mfma_f32_32x32x16_bf16 v[0:15], v[170:173], v[106:109], v[0:15]
	v_add_u32_e32 v215, v131, v89
	v_add_u32_e32 v216, v131, v90
	ds_read_b64 v[202:203], v215
	ds_read_b64 v[204:205], v216
	s_waitcnt lgkmcnt(10)
	v_mfma_f32_32x32x16_bf16 v[32:47], v[174:177], v[52:55], v[32:47]
	s_add_i32 s2, s5, 1
	s_cmp_lg_u32 s5, 5
	s_cselect_b32 s5, s2, 0
	s_mul_i32 s2, s5, 0x3800
	v_add3_u32 v126, s2, v78, v77
	s_waitcnt lgkmcnt(4)
	v_mfma_f32_32x32x16_bf16 v[32:47], v[194:197], v[48:51], v[32:47]
	v_add3_u32 v127, s2, v76, v77
	v_add3_u32 v128, s2, v79, v77
	v_add_u32_e32 v129, s2, v80
	v_add_u32_e32 v130, s2, v81
	v_add_u32_e32 v131, s2, v82
	v_mfma_f32_32x32x16_bf16 v[16:31], v[178:181], v[52:55], v[16:31]
	v_add_u32_e32 v132, v129, v83
	v_add_u32_e32 v212, v129, v84
	v_add_u32_e32 v213, v130, v83
	v_add_u32_e32 v214, v130, v84
	v_mfma_f32_32x32x16_bf16 v[0:15], v[182:185], v[52:55], v[0:15]
	v_add_u32_e32 v217, s4, v92
	s_add_i32 s4, s4, -16
	v_cndmask_b32_e32 v210, v217, v101, vcc
	v_ashrrev_i32_e32 v211, 31, v210
	v_lshl_add_u64 v[210:211], s[52:53], 0, v[210:211]
	s_waitcnt lgkmcnt(2)
	v_mfma_f32_32x32x16_bf16 v[16:31], v[198:201], v[48:51], v[16:31]
	v_add_u32_e32 v101, 16, v101
	v_lshlrev_b64 v[210:211], 10, v[210:211]
	v_lshl_add_u64 v[210:211], v[74:75], 0, v[210:211]
	v_add_u32_e32 v217, 0x15000, v56
	v_cvt_pk_bf16_f32 v32, v32, s0
	v_cvt_pk_bf16_f32 v33, v33, s0
	v_cvt_pk_bf16_f32 v34, v34, s0
	v_cvt_pk_bf16_f32 v35, v35, s0
	v_cvt_pk_bf16_f32 v36, v36, s0
	v_cvt_pk_bf16_f32 v37, v37, s0
	v_cvt_pk_bf16_f32 v38, v38, s0
	v_cvt_pk_bf16_f32 v39, v39, s0
	s_waitcnt lgkmcnt(0)
	v_mfma_f32_32x32x16_bf16 v[0:15], v[202:205], v[48:51], v[0:15]
	ds_write_b16 v93, v32
	ds_write_b16 v94, v33
	ds_write_b16 v95, v34
	ds_write_b16 v96, v35
	ds_write_b16 v97, v36
	ds_write_b16 v98, v37
	ds_write_b16 v99, v38
	ds_write_b16 v100, v39
	ds_read_b128 v[206:209], v217
	s_cmp_eq_u32 s4, -1
	s_cbranch_scc0 .LBB0_756
	s_waitcnt lgkmcnt(0)
	global_store_dwordx4 v[210:211], v[206:209], off
	s_waitcnt vmcnt(0)
	s_waitcnt lgkmcnt(0)
	s_mov_b64 s[4:5], 0
	s_barrier
